# v089 + accumulator-stationary MFMA order also in the P3 K-loop (shifted-tuple accumulators kept as exact chains)
# speedup vs baseline: 1.0040x; 1.0001x over previous
.LBB0_563:
	v_add_u32_e32 v3, 0x10000, v209
	ds_read_b128 v[140:143], v3
	ds_read_b128 v[144:147], v3 offset:1024
	ds_read_b128 v[148:151], v3 offset:2048
	ds_read_b128 v[152:155], v3 offset:3072
	v_add_u32_e32 v3, 0x14000, v209
	ds_read_b128 v[156:159], v3
	ds_read_b128 v[160:163], v3 offset:1024
	ds_read_b128 v[164:167], v3 offset:2048
	ds_read_b128 v[168:171], v3 offset:3072
	s_add_i32 s10, s57, 0xfff80080
	s_cmp_eq_u32 s59, 12
	s_cselect_b32 s62, s2, s10
	s_cselect_b32 s61, s3, s58
	s_add_i32 s60, s62, 0x80
	s_mov_b32 m0, s44
	ds_read_b128 v[172:175], v210
	ds_read_b128 v[176:179], v210 offset:1024
	ds_read_b128 v[180:183], v210 offset:2048
	ds_read_b128 v[184:187], v210 offset:3072
	ds_read_b128 v[188:191], v210 offset:4096
	ds_read_b128 v[192:195], v210 offset:5120
	ds_read_b128 v[196:199], v210 offset:6144
	ds_read_b128 v[200:203], v210 offset:7168
	buffer_load_dwordx4 v1, s[4:7], s57 offen lds
	s_mov_b32 m0, s45
	s_nop 0
	buffer_load_dwordx4 v206, s[4:7], s57 offen lds
	s_waitcnt vmcnt(8)
	s_waitcnt lgkmcnt(0)
	s_barrier
	s_waitcnt lgkmcnt(7)
	v_mfma_f32_16x16x32_bf16 v[130:133], v[140:143], v[172:175], v[130:133]
	v_mfma_f32_16x16x32_bf16 v[130:133], v[144:147], v[176:179], v[130:133]
	s_waitcnt lgkmcnt(5)
	v_mfma_f32_16x16x32_bf16 v[126:129], v[148:151], v[172:175], v[126:129]
	v_mfma_f32_16x16x32_bf16 v[126:129], v[152:155], v[176:179], v[126:129]
	s_waitcnt lgkmcnt(3)
	v_mfma_f32_16x16x32_bf16 v[122:125], v[140:143], v[180:183], v[122:125]
	v_mfma_f32_16x16x32_bf16 v[122:125], v[144:147], v[184:187], v[122:125]
	s_waitcnt lgkmcnt(1)
	v_mfma_f32_16x16x32_bf16 v[118:121], v[148:151], v[180:183], v[118:121]
	v_mfma_f32_16x16x32_bf16 v[118:121], v[152:155], v[184:187], v[118:121]
	v_mfma_f32_16x16x32_bf16 v[114:117], v[140:143], v[188:191], v[114:117]
	v_mfma_f32_16x16x32_bf16 v[114:117], v[144:147], v[192:195], v[114:117]
	v_mfma_f32_16x16x32_bf16 v[110:113], v[148:151], v[188:191], v[110:113]
	v_mfma_f32_16x16x32_bf16 v[110:113], v[152:155], v[192:195], v[110:113]
	v_mfma_f32_16x16x32_bf16 v[106:109], v[140:143], v[196:199], v[106:109]
	v_mfma_f32_16x16x32_bf16 v[106:109], v[144:147], v[200:203], v[106:109]
	s_waitcnt lgkmcnt(0)
	v_mfma_f32_16x16x32_bf16 v[102:105], v[148:151], v[196:199], v[102:105]
	v_mfma_f32_16x16x32_bf16 v[102:105], v[152:155], v[200:203], v[102:105]
	v_mfma_f32_16x16x32_bf16 v[98:101], v[156:159], v[172:175], v[98:101]
	v_mfma_f32_16x16x32_bf16 v[98:101], v[160:163], v[176:179], v[98:101]
	v_mfma_f32_16x16x32_bf16 v[94:97], v[164:167], v[172:175], v[94:97]
	v_mfma_f32_16x16x32_bf16 v[94:97], v[168:171], v[176:179], v[94:97]
	v_mfma_f32_16x16x32_bf16 v[90:93], v[156:159], v[180:183], v[90:93]
	v_mfma_f32_16x16x32_bf16 v[90:93], v[160:163], v[184:187], v[90:93]
	v_mfma_f32_16x16x32_bf16 v[86:89], v[164:167], v[180:183], v[86:89]
	v_mfma_f32_16x16x32_bf16 v[86:89], v[168:171], v[184:187], v[86:89]
	v_mfma_f32_16x16x32_bf16 v[82:85], v[156:159], v[188:191], v[82:85]
	v_mfma_f32_16x16x32_bf16 v[82:85], v[160:163], v[192:195], v[82:85]
	v_mfma_f32_16x16x32_bf16 v[78:81], v[164:167], v[188:191], v[78:81]
	v_mfma_f32_16x16x32_bf16 v[78:81], v[168:171], v[192:195], v[78:81]
	v_mfma_f32_16x16x32_bf16 v[74:77], v[156:159], v[196:199], v[74:77]
	v_mfma_f32_16x16x32_bf16 v[74:77], v[160:163], v[200:203], v[74:77]
	v_mfma_f32_16x16x32_bf16 v[70:73], v[164:167], v[196:199], v[70:73]
	v_mfma_f32_16x16x32_bf16 v[70:73], v[168:171], v[200:203], v[70:73]
	s_barrier
	s_mov_b32 m0, s28
	s_mov_b32 s10, s6
	s_mov_b32 s11, s7
	ds_read_b128 v[172:175], v210 offset:16384
	ds_read_b128 v[176:179], v210 offset:17408
	ds_read_b128 v[180:183], v210 offset:18432
	ds_read_b128 v[184:187], v210 offset:19456
	ds_read_b128 v[188:191], v210 offset:20480
	ds_read_b128 v[192:195], v210 offset:21504
	ds_read_b128 v[196:199], v210 offset:22528
	ds_read_b128 v[200:203], v210 offset:23552
	buffer_load_dwordx4 v135, s[8:11], s61 offen lds
	s_mov_b32 m0, s29
	s_add_i32 s63, s61, 0x80000
	buffer_load_dwordx4 v207, s[8:11], s61 offen lds
	s_mov_b32 m0, s30
	s_nop 0
	buffer_load_dwordx4 v135, s[8:11], s63 offen lds
	s_mov_b32 m0, s31
	s_nop 0
	buffer_load_dwordx4 v207, s[8:11], s63 offen lds
	s_mov_b32 m0, s27
	s_nop 0
	buffer_load_dwordx4 v1, s[4:7], s62 offen lds
	s_mov_b32 m0, s33
	s_nop 0
	buffer_load_dwordx4 v206, s[4:7], s62 offen lds
	s_waitcnt vmcnt(8)
	s_waitcnt lgkmcnt(0)
	s_barrier
	s_waitcnt lgkmcnt(7)
	v_mfma_f32_16x16x32_bf16 v[66:69], v[140:143], v[172:175], v[66:69]
	v_mfma_f32_16x16x32_bf16 v[66:69], v[144:147], v[176:179], v[66:69]
	s_waitcnt lgkmcnt(5)
	v_mfma_f32_16x16x32_bf16 v[62:65], v[148:151], v[172:175], v[62:65]
	v_mfma_f32_16x16x32_bf16 v[62:65], v[152:155], v[176:179], v[62:65]
	s_waitcnt lgkmcnt(3)
	v_mfma_f32_16x16x32_bf16 v[58:61], v[140:143], v[180:183], v[58:61]
	v_mfma_f32_16x16x32_bf16 v[58:61], v[144:147], v[184:187], v[58:61]
	s_waitcnt lgkmcnt(1)
	v_mfma_f32_16x16x32_bf16 v[54:57], v[148:151], v[180:183], v[54:57]
	v_mfma_f32_16x16x32_bf16 v[54:57], v[152:155], v[184:187], v[54:57]
	v_mfma_f32_16x16x32_bf16 v[50:53], v[140:143], v[188:191], v[50:53]
	v_mfma_f32_16x16x32_bf16 v[50:53], v[144:147], v[192:195], v[50:53]
	v_mfma_f32_16x16x32_bf16 v[46:49], v[148:151], v[188:191], v[46:49]
	v_mfma_f32_16x16x32_bf16 v[46:49], v[152:155], v[192:195], v[46:49]
	v_mfma_f32_16x16x32_bf16 v[42:45], v[140:143], v[196:199], v[42:45]
	v_mfma_f32_16x16x32_bf16 v[42:45], v[144:147], v[200:203], v[42:45]
	s_waitcnt lgkmcnt(0)
	v_mfma_f32_16x16x32_bf16 v[38:41], v[148:151], v[196:199], v[38:41]
	v_mfma_f32_16x16x32_bf16 v[38:41], v[152:155], v[200:203], v[38:41]
	v_mfma_f32_16x16x32_bf16 v[34:37], v[156:159], v[172:175], v[34:37]
	v_mfma_f32_16x16x32_bf16 v[34:37], v[160:163], v[176:179], v[34:37]
	v_mfma_f32_16x16x32_bf16 v[30:33], v[164:167], v[172:175], v[30:33]
	v_mfma_f32_16x16x32_bf16 v[30:33], v[168:171], v[176:179], v[30:33]
	v_mfma_f32_16x16x32_bf16 v[26:29], v[156:159], v[180:183], v[26:29]
	v_mfma_f32_16x16x32_bf16 v[26:29], v[160:163], v[184:187], v[26:29]
	v_mfma_f32_16x16x32_bf16 v[22:25], v[164:167], v[180:183], v[22:25]
	v_mfma_f32_16x16x32_bf16 v[22:25], v[168:171], v[184:187], v[22:25]
	v_mfma_f32_16x16x32_bf16 v[18:21], v[156:159], v[188:191], v[18:21]
	v_mfma_f32_16x16x32_bf16 v[18:21], v[160:163], v[192:195], v[18:21]
	v_mfma_f32_16x16x32_bf16 v[14:17], v[164:167], v[188:191], v[14:17]
	v_mfma_f32_16x16x32_bf16 v[14:17], v[168:171], v[192:195], v[14:17]
	v_mfma_f32_16x16x32_bf16 v[10:13], v[156:159], v[196:199], v[10:13]
	v_mfma_f32_16x16x32_bf16 v[10:13], v[160:163], v[200:203], v[10:13]
	v_mfma_f32_16x16x32_bf16 v[4:7], v[164:167], v[196:199], v[6:9]
	v_mfma_f32_16x16x32_bf16 v[4:7], v[168:171], v[200:203], v[4:7]
	s_barrier
	v_add_u32_e32 v3, 0x18000, v209
	ds_read_b128 v[140:143], v3
	ds_read_b128 v[144:147], v3 offset:1024
	ds_read_b128 v[148:151], v3 offset:2048
	ds_read_b128 v[152:155], v3 offset:3072
	v_add_u32_e32 v3, 0x1c000, v209
	ds_read_b128 v[156:159], v3
	ds_read_b128 v[160:163], v3 offset:1024
	ds_read_b128 v[164:167], v3 offset:2048
	ds_read_b128 v[168:171], v3 offset:3072
	s_add_i32 s62, s62, 0x80000
	s_mov_b32 m0, s34
	ds_read_b128 v[172:175], v210 offset:32768
	ds_read_b128 v[176:179], v210 offset:33792
	ds_read_b128 v[180:183], v210 offset:34816
	ds_read_b128 v[184:187], v210 offset:35840
	ds_read_b128 v[188:191], v210 offset:36864
	ds_read_b128 v[192:195], v210 offset:37888
	ds_read_b128 v[196:199], v210 offset:38912
	ds_read_b128 v[200:203], v210 offset:39936
	buffer_load_dwordx4 v1, s[4:7], s62 offen lds
	s_mov_b32 m0, s35
	s_nop 0
	buffer_load_dwordx4 v206, s[4:7], s62 offen lds
	s_waitcnt vmcnt(8)
	s_waitcnt lgkmcnt(0)
	s_barrier
	s_waitcnt lgkmcnt(7)
	v_mfma_f32_16x16x32_bf16 v[130:133], v[140:143], v[172:175], v[130:133]
	v_mfma_f32_16x16x32_bf16 v[130:133], v[144:147], v[176:179], v[130:133]
	s_waitcnt lgkmcnt(5)
	v_mfma_f32_16x16x32_bf16 v[126:129], v[148:151], v[172:175], v[126:129]
	v_mfma_f32_16x16x32_bf16 v[126:129], v[152:155], v[176:179], v[126:129]
	s_waitcnt lgkmcnt(3)
	v_mfma_f32_16x16x32_bf16 v[122:125], v[140:143], v[180:183], v[122:125]
	v_mfma_f32_16x16x32_bf16 v[122:125], v[144:147], v[184:187], v[122:125]
	s_waitcnt lgkmcnt(1)
	v_mfma_f32_16x16x32_bf16 v[118:121], v[148:151], v[180:183], v[118:121]
	v_mfma_f32_16x16x32_bf16 v[118:121], v[152:155], v[184:187], v[118:121]
	v_mfma_f32_16x16x32_bf16 v[114:117], v[140:143], v[188:191], v[114:117]
	v_mfma_f32_16x16x32_bf16 v[114:117], v[144:147], v[192:195], v[114:117]
	v_mfma_f32_16x16x32_bf16 v[110:113], v[148:151], v[188:191], v[110:113]
	v_mfma_f32_16x16x32_bf16 v[110:113], v[152:155], v[192:195], v[110:113]
	v_mfma_f32_16x16x32_bf16 v[106:109], v[140:143], v[196:199], v[106:109]
	v_mfma_f32_16x16x32_bf16 v[106:109], v[144:147], v[200:203], v[106:109]
	s_waitcnt lgkmcnt(0)
	v_mfma_f32_16x16x32_bf16 v[102:105], v[148:151], v[196:199], v[102:105]
	v_mfma_f32_16x16x32_bf16 v[102:105], v[152:155], v[200:203], v[102:105]
	v_mfma_f32_16x16x32_bf16 v[98:101], v[156:159], v[172:175], v[98:101]
	v_mfma_f32_16x16x32_bf16 v[98:101], v[160:163], v[176:179], v[98:101]
	v_mfma_f32_16x16x32_bf16 v[94:97], v[164:167], v[172:175], v[94:97]
	v_mfma_f32_16x16x32_bf16 v[94:97], v[168:171], v[176:179], v[94:97]
	v_mfma_f32_16x16x32_bf16 v[90:93], v[156:159], v[180:183], v[90:93]
	v_mfma_f32_16x16x32_bf16 v[90:93], v[160:163], v[184:187], v[90:93]
	v_mfma_f32_16x16x32_bf16 v[86:89], v[164:167], v[180:183], v[86:89]
	v_mfma_f32_16x16x32_bf16 v[86:89], v[168:171], v[184:187], v[86:89]
	v_mfma_f32_16x16x32_bf16 v[82:85], v[156:159], v[188:191], v[82:85]
	v_mfma_f32_16x16x32_bf16 v[82:85], v[160:163], v[192:195], v[82:85]
	v_mfma_f32_16x16x32_bf16 v[78:81], v[164:167], v[188:191], v[78:81]
	v_mfma_f32_16x16x32_bf16 v[78:81], v[168:171], v[192:195], v[78:81]
	v_mfma_f32_16x16x32_bf16 v[74:77], v[156:159], v[196:199], v[74:77]
	v_mfma_f32_16x16x32_bf16 v[74:77], v[160:163], v[200:203], v[74:77]
	v_mfma_f32_16x16x32_bf16 v[70:73], v[164:167], v[196:199], v[70:73]
	v_mfma_f32_16x16x32_bf16 v[70:73], v[168:171], v[200:203], v[70:73]
	s_barrier
	s_mov_b32 m0, s38
	s_add_i32 s62, s61, 0x80
	ds_read_b128 v[172:175], v210 offset:49152
	ds_read_b128 v[176:179], v210 offset:50176
	ds_read_b128 v[180:183], v210 offset:51200
	ds_read_b128 v[184:187], v210 offset:52224
	ds_read_b128 v[188:191], v210 offset:53248
	ds_read_b128 v[192:195], v210 offset:54272
	ds_read_b128 v[196:199], v210 offset:55296
	ds_read_b128 v[200:203], v210 offset:56320
	buffer_load_dwordx4 v135, s[8:11], s62 offen lds
	s_mov_b32 m0, s39
	s_add_i32 s61, s61, 0x80080
	buffer_load_dwordx4 v207, s[8:11], s62 offen lds
	s_mov_b32 m0, s42
	s_nop 0
	buffer_load_dwordx4 v135, s[8:11], s61 offen lds
	s_mov_b32 m0, s43
	s_nop 0
	buffer_load_dwordx4 v207, s[8:11], s61 offen lds
	s_mov_b32 m0, s40
	s_nop 0
	buffer_load_dwordx4 v1, s[4:7], s60 offen lds
	s_mov_b32 m0, s41
	s_nop 0
	buffer_load_dwordx4 v206, s[4:7], s60 offen lds
	s_waitcnt vmcnt(8)
	s_waitcnt lgkmcnt(0)
	s_barrier
	s_waitcnt lgkmcnt(7)
	v_mfma_f32_16x16x32_bf16 v[66:69], v[140:143], v[172:175], v[66:69]
	v_mfma_f32_16x16x32_bf16 v[66:69], v[144:147], v[176:179], v[66:69]
	s_waitcnt lgkmcnt(5)
	v_mfma_f32_16x16x32_bf16 v[62:65], v[148:151], v[172:175], v[62:65]
	v_mfma_f32_16x16x32_bf16 v[62:65], v[152:155], v[176:179], v[62:65]
	s_waitcnt lgkmcnt(3)
	v_mfma_f32_16x16x32_bf16 v[58:61], v[140:143], v[180:183], v[58:61]
	v_mfma_f32_16x16x32_bf16 v[58:61], v[144:147], v[184:187], v[58:61]
	s_waitcnt lgkmcnt(1)
	v_mfma_f32_16x16x32_bf16 v[54:57], v[148:151], v[180:183], v[54:57]
	v_mfma_f32_16x16x32_bf16 v[54:57], v[152:155], v[184:187], v[54:57]
	v_mfma_f32_16x16x32_bf16 v[50:53], v[140:143], v[188:191], v[50:53]
	v_mfma_f32_16x16x32_bf16 v[50:53], v[144:147], v[192:195], v[50:53]
	v_mfma_f32_16x16x32_bf16 v[46:49], v[148:151], v[188:191], v[46:49]
	v_mfma_f32_16x16x32_bf16 v[46:49], v[152:155], v[192:195], v[46:49]
	v_mfma_f32_16x16x32_bf16 v[42:45], v[140:143], v[196:199], v[42:45]
	v_mfma_f32_16x16x32_bf16 v[42:45], v[144:147], v[200:203], v[42:45]
	s_waitcnt lgkmcnt(0)
	v_mfma_f32_16x16x32_bf16 v[38:41], v[148:151], v[196:199], v[38:41]
	v_mfma_f32_16x16x32_bf16 v[38:41], v[152:155], v[200:203], v[38:41]
	v_mfma_f32_16x16x32_bf16 v[34:37], v[156:159], v[172:175], v[34:37]
	v_mfma_f32_16x16x32_bf16 v[34:37], v[160:163], v[176:179], v[34:37]
	v_mfma_f32_16x16x32_bf16 v[30:33], v[164:167], v[172:175], v[30:33]
	v_mfma_f32_16x16x32_bf16 v[30:33], v[168:171], v[176:179], v[30:33]
	v_mfma_f32_16x16x32_bf16 v[26:29], v[156:159], v[180:183], v[26:29]
	v_mfma_f32_16x16x32_bf16 v[26:29], v[160:163], v[184:187], v[26:29]
	v_mfma_f32_16x16x32_bf16 v[22:25], v[164:167], v[180:183], v[22:25]
	v_mfma_f32_16x16x32_bf16 v[22:25], v[168:171], v[184:187], v[22:25]
	v_mfma_f32_16x16x32_bf16 v[18:21], v[156:159], v[188:191], v[18:21]
	v_mfma_f32_16x16x32_bf16 v[18:21], v[160:163], v[192:195], v[18:21]
	v_mfma_f32_16x16x32_bf16 v[14:17], v[164:167], v[188:191], v[14:17]
	v_mfma_f32_16x16x32_bf16 v[14:17], v[168:171], v[192:195], v[14:17]
	v_mfma_f32_16x16x32_bf16 v[8:11], v[156:159], v[196:199], v[10:13]
	v_mfma_f32_16x16x32_bf16 v[10:13], v[160:163], v[200:203], v[8:11]
	v_mfma_f32_16x16x32_bf16 v[4:7], v[164:167], v[196:199], v[4:7]
	v_mfma_f32_16x16x32_bf16 v[6:9], v[168:171], v[200:203], v[4:7]
	s_barrier
	s_add_i32 s59, s59, 2
	s_addk_i32 s57, 0x100
	s_addk_i32 s58, 0x100
	s_cmp_gt_u32 s59, 13
	s_cbranch_scc0 .LBB0_563
	s_and_b64 vcc, exec, s[20:21]
	s_cbranch_vccz .LBB0_566
	s_barrier
